# adaLN silu(c) staging loop de-serialised (34 loads in flight, counted waits) on top of K-loop peel and SwiGLU epilogue rewrite
# baseline (speedup 1.0000x reference)
.LBB0_7:
	s_lshr_b32 s4, s10, 6
	s_load_dwordx16 s[36:51], s[0:1], 0x0
	s_load_dwordx16 s[52:67], s[0:1], 0x40
	s_load_dwordx16 s[12:27], s[0:1], 0x80
	v_writelane_b32 v254, s10, 5
	s_lshl_b32 s1, s2, 3
	s_mov_b32 s0, s4
	v_writelane_b32 v254, s0, 6
	s_add_i32 s97, s4, s1
	v_and_b32_e32 v250, 63, v0
	v_writelane_b32 v254, s1, 7
	s_lshl_b32 s0, s28, 3
	v_writelane_b32 v254, s1, 8
	s_cmp_lt_i32 s74, 1
	v_writelane_b32 v254, s0, 9
	s_cselect_b64 s[0:1], -1, 0
	s_cmp_gt_i32 s75, 0
	s_cselect_b64 s[4:5], -1, 0
	s_and_b64 s[0:1], s[0:1], s[4:5]
	s_andn2_b64 vcc, exec, s[0:1]
	s_cbranch_vccnz .LBB0_77
	s_cmpk_gt_i32 s2, 0xbf
	s_cbranch_scc1 .LBB0_50
	v_lshlrev_b32_e32 v2, 2, v0
	s_waitcnt lgkmcnt(0)
	v_add_u32_e32 v1, 0, v2
	v_add_u32_e32 v3, 0x10000, v2
	s_mov_b64 s[4:5], s[38:39]
	global_load_dword v20, v2, s[4:5]
	global_load_dword v21, v2, s[4:5] offset:2048
	s_add_u32 s4, s4, 0x1000
	s_addc_u32 s5, s5, 0
	global_load_dword v22, v2, s[4:5]
	global_load_dword v23, v2, s[4:5] offset:2048
	s_add_u32 s4, s4, 0x1000
	s_addc_u32 s5, s5, 0
	global_load_dword v24, v2, s[4:5]
	global_load_dword v25, v2, s[4:5] offset:2048
	s_add_u32 s4, s4, 0x1000
	s_addc_u32 s5, s5, 0
	global_load_dword v26, v2, s[4:5]
	global_load_dword v27, v2, s[4:5] offset:2048
	s_add_u32 s4, s4, 0x1000
	s_addc_u32 s5, s5, 0
	global_load_dword v28, v2, s[4:5]
	global_load_dword v29, v2, s[4:5] offset:2048
	s_add_u32 s4, s4, 0x1000
	s_addc_u32 s5, s5, 0
	global_load_dword v30, v2, s[4:5]
	global_load_dword v31, v2, s[4:5] offset:2048
	s_add_u32 s4, s4, 0x1000
	s_addc_u32 s5, s5, 0
	global_load_dword v32, v2, s[4:5]
	global_load_dword v33, v2, s[4:5] offset:2048
	s_add_u32 s4, s4, 0x1000
	s_addc_u32 s5, s5, 0
	global_load_dword v34, v2, s[4:5]
	global_load_dword v35, v2, s[4:5] offset:2048
	s_add_u32 s4, s4, 0x1000
	s_addc_u32 s5, s5, 0
	global_load_dword v36, v2, s[4:5]
	global_load_dword v37, v2, s[4:5] offset:2048
	s_add_u32 s4, s4, 0x1000
	s_addc_u32 s5, s5, 0
	global_load_dword v38, v2, s[4:5]
	global_load_dword v39, v2, s[4:5] offset:2048
	s_add_u32 s4, s4, 0x1000
	s_addc_u32 s5, s5, 0
	global_load_dword v40, v2, s[4:5]
	global_load_dword v41, v2, s[4:5] offset:2048
	s_add_u32 s4, s4, 0x1000
	s_addc_u32 s5, s5, 0
	global_load_dword v42, v2, s[4:5]
	global_load_dword v43, v2, s[4:5] offset:2048
	s_add_u32 s4, s4, 0x1000
	s_addc_u32 s5, s5, 0
	global_load_dword v44, v2, s[4:5]
	global_load_dword v45, v2, s[4:5] offset:2048
	s_add_u32 s4, s4, 0x1000
	s_addc_u32 s5, s5, 0
	global_load_dword v46, v2, s[4:5]
	global_load_dword v47, v2, s[4:5] offset:2048
	s_add_u32 s4, s4, 0x1000
	s_addc_u32 s5, s5, 0
	global_load_dword v48, v2, s[4:5]
	global_load_dword v49, v2, s[4:5] offset:2048
	s_add_u32 s4, s4, 0x1000
	s_addc_u32 s5, s5, 0
	global_load_dword v50, v2, s[4:5]
	global_load_dword v51, v2, s[4:5] offset:2048
	global_load_dword v52, v2, s[42:43]
	global_load_dword v53, v2, s[42:43] offset:2048
	s_waitcnt vmcnt(33)
	v_mul_f32_e32 v8, 0xbfb8aa3b, v20
	v_exp_f32_e32 v8, v8
	s_nop 0
	v_add_f32_e32 v8, 1.0, v8
	v_div_scale_f32 v9, s[10:11], v8, v8, v20
	v_rcp_f32_e32 v10, v9
	v_div_scale_f32 v11, vcc, v20, v8, v20
	v_fma_f32 v12, -v9, v10, 1.0
	v_fmac_f32_e32 v10, v12, v10
	v_mul_f32_e32 v12, v11, v10
	v_fma_f32 v13, -v9, v12, v11
	v_fmac_f32_e32 v12, v13, v10
	v_fma_f32 v9, -v9, v12, v11
	v_div_fmas_f32 v9, v9, v10, v12
	v_div_fixup_f32 v20, v9, v8, v20
	ds_write_b32 v1, v20
	s_waitcnt vmcnt(32)
	v_mul_f32_e32 v8, 0xbfb8aa3b, v21
	v_exp_f32_e32 v8, v8
	s_nop 0
	v_add_f32_e32 v8, 1.0, v8
	v_div_scale_f32 v9, s[10:11], v8, v8, v21
	v_rcp_f32_e32 v10, v9
	v_div_scale_f32 v11, vcc, v21, v8, v21
	v_fma_f32 v12, -v9, v10, 1.0
	v_fmac_f32_e32 v10, v12, v10
	v_mul_f32_e32 v12, v11, v10
	v_fma_f32 v13, -v9, v12, v11
	v_fmac_f32_e32 v12, v13, v10
	v_fma_f32 v9, -v9, v12, v11
	v_div_fmas_f32 v9, v9, v10, v12
	v_div_fixup_f32 v21, v9, v8, v21
	ds_write_b32 v1, v21 offset:2048
	s_waitcnt vmcnt(31)
	v_mul_f32_e32 v8, 0xbfb8aa3b, v22
	v_exp_f32_e32 v8, v8
	s_nop 0
	v_add_f32_e32 v8, 1.0, v8
	v_div_scale_f32 v9, s[10:11], v8, v8, v22
	v_rcp_f32_e32 v10, v9
	v_div_scale_f32 v11, vcc, v22, v8, v22
	v_fma_f32 v12, -v9, v10, 1.0
	v_fmac_f32_e32 v10, v12, v10
	v_mul_f32_e32 v12, v11, v10
	v_fma_f32 v13, -v9, v12, v11
	v_fmac_f32_e32 v12, v13, v10
	v_fma_f32 v9, -v9, v12, v11
	v_div_fmas_f32 v9, v9, v10, v12
	v_div_fixup_f32 v22, v9, v8, v22
	ds_write_b32 v1, v22 offset:4096
	s_waitcnt vmcnt(30)
	v_mul_f32_e32 v8, 0xbfb8aa3b, v23
	v_exp_f32_e32 v8, v8
	s_nop 0
	v_add_f32_e32 v8, 1.0, v8
	v_div_scale_f32 v9, s[10:11], v8, v8, v23
	v_rcp_f32_e32 v10, v9
	v_div_scale_f32 v11, vcc, v23, v8, v23
	v_fma_f32 v12, -v9, v10, 1.0
	v_fmac_f32_e32 v10, v12, v10
	v_mul_f32_e32 v12, v11, v10
	v_fma_f32 v13, -v9, v12, v11
	v_fmac_f32_e32 v12, v13, v10
	v_fma_f32 v9, -v9, v12, v11
	v_div_fmas_f32 v9, v9, v10, v12
	v_div_fixup_f32 v23, v9, v8, v23
	ds_write_b32 v1, v23 offset:6144
	s_waitcnt vmcnt(29)
	v_mul_f32_e32 v8, 0xbfb8aa3b, v24
	v_exp_f32_e32 v8, v8
	s_nop 0
	v_add_f32_e32 v8, 1.0, v8
	v_div_scale_f32 v9, s[10:11], v8, v8, v24
	v_rcp_f32_e32 v10, v9
	v_div_scale_f32 v11, vcc, v24, v8, v24
	v_fma_f32 v12, -v9, v10, 1.0
	v_fmac_f32_e32 v10, v12, v10
	v_mul_f32_e32 v12, v11, v10
	v_fma_f32 v13, -v9, v12, v11
	v_fmac_f32_e32 v12, v13, v10
	v_fma_f32 v9, -v9, v12, v11
	v_div_fmas_f32 v9, v9, v10, v12
	v_div_fixup_f32 v24, v9, v8, v24
	ds_write_b32 v1, v24 offset:8192
	s_waitcnt vmcnt(28)
	v_mul_f32_e32 v8, 0xbfb8aa3b, v25
	v_exp_f32_e32 v8, v8
	s_nop 0
	v_add_f32_e32 v8, 1.0, v8
	v_div_scale_f32 v9, s[10:11], v8, v8, v25
	v_rcp_f32_e32 v10, v9
	v_div_scale_f32 v11, vcc, v25, v8, v25
	v_fma_f32 v12, -v9, v10, 1.0
	v_fmac_f32_e32 v10, v12, v10
	v_mul_f32_e32 v12, v11, v10
	v_fma_f32 v13, -v9, v12, v11
	v_fmac_f32_e32 v12, v13, v10
	v_fma_f32 v9, -v9, v12, v11
	v_div_fmas_f32 v9, v9, v10, v12
	v_div_fixup_f32 v25, v9, v8, v25
	ds_write_b32 v1, v25 offset:10240
	s_waitcnt vmcnt(27)
	v_mul_f32_e32 v8, 0xbfb8aa3b, v26
	v_exp_f32_e32 v8, v8
	s_nop 0
	v_add_f32_e32 v8, 1.0, v8
	v_div_scale_f32 v9, s[10:11], v8, v8, v26
	v_rcp_f32_e32 v10, v9
	v_div_scale_f32 v11, vcc, v26, v8, v26
	v_fma_f32 v12, -v9, v10, 1.0
	v_fmac_f32_e32 v10, v12, v10
	v_mul_f32_e32 v12, v11, v10
	v_fma_f32 v13, -v9, v12, v11
	v_fmac_f32_e32 v12, v13, v10
	v_fma_f32 v9, -v9, v12, v11
	v_div_fmas_f32 v9, v9, v10, v12
	v_div_fixup_f32 v26, v9, v8, v26
	ds_write_b32 v1, v26 offset:12288
	s_waitcnt vmcnt(26)
	v_mul_f32_e32 v8, 0xbfb8aa3b, v27
	v_exp_f32_e32 v8, v8
	s_nop 0
	v_add_f32_e32 v8, 1.0, v8
	v_div_scale_f32 v9, s[10:11], v8, v8, v27
	v_rcp_f32_e32 v10, v9
	v_div_scale_f32 v11, vcc, v27, v8, v27
	v_fma_f32 v12, -v9, v10, 1.0
	v_fmac_f32_e32 v10, v12, v10
	v_mul_f32_e32 v12, v11, v10
	v_fma_f32 v13, -v9, v12, v11
	v_fmac_f32_e32 v12, v13, v10
	v_fma_f32 v9, -v9, v12, v11
	v_div_fmas_f32 v9, v9, v10, v12
	v_div_fixup_f32 v27, v9, v8, v27
	ds_write_b32 v1, v27 offset:14336
	s_waitcnt vmcnt(25)
	v_mul_f32_e32 v8, 0xbfb8aa3b, v28
	v_exp_f32_e32 v8, v8
	s_nop 0
	v_add_f32_e32 v8, 1.0, v8
	v_div_scale_f32 v9, s[10:11], v8, v8, v28
	v_rcp_f32_e32 v10, v9
	v_div_scale_f32 v11, vcc, v28, v8, v28
	v_fma_f32 v12, -v9, v10, 1.0
	v_fmac_f32_e32 v10, v12, v10
	v_mul_f32_e32 v12, v11, v10
	v_fma_f32 v13, -v9, v12, v11
	v_fmac_f32_e32 v12, v13, v10
	v_fma_f32 v9, -v9, v12, v11
	v_div_fmas_f32 v9, v9, v10, v12
	v_div_fixup_f32 v28, v9, v8, v28
	ds_write_b32 v1, v28 offset:16384
	s_waitcnt vmcnt(24)
	v_mul_f32_e32 v8, 0xbfb8aa3b, v29
	v_exp_f32_e32 v8, v8
	s_nop 0
	v_add_f32_e32 v8, 1.0, v8
	v_div_scale_f32 v9, s[10:11], v8, v8, v29
	v_rcp_f32_e32 v10, v9
	v_div_scale_f32 v11, vcc, v29, v8, v29
	v_fma_f32 v12, -v9, v10, 1.0
	v_fmac_f32_e32 v10, v12, v10
	v_mul_f32_e32 v12, v11, v10
	v_fma_f32 v13, -v9, v12, v11
	v_fmac_f32_e32 v12, v13, v10
	v_fma_f32 v9, -v9, v12, v11
	v_div_fmas_f32 v9, v9, v10, v12
	v_div_fixup_f32 v29, v9, v8, v29
	ds_write_b32 v1, v29 offset:18432
	s_waitcnt vmcnt(23)
	v_mul_f32_e32 v8, 0xbfb8aa3b, v30
	v_exp_f32_e32 v8, v8
	s_nop 0
	v_add_f32_e32 v8, 1.0, v8
	v_div_scale_f32 v9, s[10:11], v8, v8, v30
	v_rcp_f32_e32 v10, v9
	v_div_scale_f32 v11, vcc, v30, v8, v30
	v_fma_f32 v12, -v9, v10, 1.0
	v_fmac_f32_e32 v10, v12, v10
	v_mul_f32_e32 v12, v11, v10
	v_fma_f32 v13, -v9, v12, v11
	v_fmac_f32_e32 v12, v13, v10
	v_fma_f32 v9, -v9, v12, v11
	v_div_fmas_f32 v9, v9, v10, v12
	v_div_fixup_f32 v30, v9, v8, v30
	ds_write_b32 v1, v30 offset:20480
	s_waitcnt vmcnt(22)
	v_mul_f32_e32 v8, 0xbfb8aa3b, v31
	v_exp_f32_e32 v8, v8
	s_nop 0
	v_add_f32_e32 v8, 1.0, v8
	v_div_scale_f32 v9, s[10:11], v8, v8, v31
	v_rcp_f32_e32 v10, v9
	v_div_scale_f32 v11, vcc, v31, v8, v31
	v_fma_f32 v12, -v9, v10, 1.0
	v_fmac_f32_e32 v10, v12, v10
	v_mul_f32_e32 v12, v11, v10
	v_fma_f32 v13, -v9, v12, v11
	v_fmac_f32_e32 v12, v13, v10
	v_fma_f32 v9, -v9, v12, v11
	v_div_fmas_f32 v9, v9, v10, v12
	v_div_fixup_f32 v31, v9, v8, v31
	ds_write_b32 v1, v31 offset:22528
	s_waitcnt vmcnt(21)
	v_mul_f32_e32 v8, 0xbfb8aa3b, v32
	v_exp_f32_e32 v8, v8
	s_nop 0
	v_add_f32_e32 v8, 1.0, v8
	v_div_scale_f32 v9, s[10:11], v8, v8, v32
	v_rcp_f32_e32 v10, v9
	v_div_scale_f32 v11, vcc, v32, v8, v32
	v_fma_f32 v12, -v9, v10, 1.0
	v_fmac_f32_e32 v10, v12, v10
	v_mul_f32_e32 v12, v11, v10
	v_fma_f32 v13, -v9, v12, v11
	v_fmac_f32_e32 v12, v13, v10
	v_fma_f32 v9, -v9, v12, v11
	v_div_fmas_f32 v9, v9, v10, v12
	v_div_fixup_f32 v32, v9, v8, v32
	ds_write_b32 v1, v32 offset:24576
	s_waitcnt vmcnt(20)
	v_mul_f32_e32 v8, 0xbfb8aa3b, v33
	v_exp_f32_e32 v8, v8
	s_nop 0
	v_add_f32_e32 v8, 1.0, v8
	v_div_scale_f32 v9, s[10:11], v8, v8, v33
	v_rcp_f32_e32 v10, v9
	v_div_scale_f32 v11, vcc, v33, v8, v33
	v_fma_f32 v12, -v9, v10, 1.0
	v_fmac_f32_e32 v10, v12, v10
	v_mul_f32_e32 v12, v11, v10
	v_fma_f32 v13, -v9, v12, v11
	v_fmac_f32_e32 v12, v13, v10
	v_fma_f32 v9, -v9, v12, v11
	v_div_fmas_f32 v9, v9, v10, v12
	v_div_fixup_f32 v33, v9, v8, v33
	ds_write_b32 v1, v33 offset:26624
	s_waitcnt vmcnt(19)
	v_mul_f32_e32 v8, 0xbfb8aa3b, v34
	v_exp_f32_e32 v8, v8
	s_nop 0
	v_add_f32_e32 v8, 1.0, v8
	v_div_scale_f32 v9, s[10:11], v8, v8, v34
	v_rcp_f32_e32 v10, v9
	v_div_scale_f32 v11, vcc, v34, v8, v34
	v_fma_f32 v12, -v9, v10, 1.0
	v_fmac_f32_e32 v10, v12, v10
	v_mul_f32_e32 v12, v11, v10
	v_fma_f32 v13, -v9, v12, v11
	v_fmac_f32_e32 v12, v13, v10
	v_fma_f32 v9, -v9, v12, v11
	v_div_fmas_f32 v9, v9, v10, v12
	v_div_fixup_f32 v34, v9, v8, v34
	ds_write_b32 v1, v34 offset:28672
	s_waitcnt vmcnt(18)
	v_mul_f32_e32 v8, 0xbfb8aa3b, v35
	v_exp_f32_e32 v8, v8
	s_nop 0
	v_add_f32_e32 v8, 1.0, v8
	v_div_scale_f32 v9, s[10:11], v8, v8, v35
	v_rcp_f32_e32 v10, v9
	v_div_scale_f32 v11, vcc, v35, v8, v35
	v_fma_f32 v12, -v9, v10, 1.0
	v_fmac_f32_e32 v10, v12, v10
	v_mul_f32_e32 v12, v11, v10
	v_fma_f32 v13, -v9, v12, v11
	v_fmac_f32_e32 v12, v13, v10
	v_fma_f32 v9, -v9, v12, v11
	v_div_fmas_f32 v9, v9, v10, v12
	v_div_fixup_f32 v35, v9, v8, v35
	ds_write_b32 v1, v35 offset:30720
	s_waitcnt vmcnt(17)
	v_mul_f32_e32 v8, 0xbfb8aa3b, v36
	v_exp_f32_e32 v8, v8
	s_nop 0
	v_add_f32_e32 v8, 1.0, v8
	v_div_scale_f32 v9, s[10:11], v8, v8, v36
	v_rcp_f32_e32 v10, v9
	v_div_scale_f32 v11, vcc, v36, v8, v36
	v_fma_f32 v12, -v9, v10, 1.0
	v_fmac_f32_e32 v10, v12, v10
	v_mul_f32_e32 v12, v11, v10
	v_fma_f32 v13, -v9, v12, v11
	v_fmac_f32_e32 v12, v13, v10
	v_fma_f32 v9, -v9, v12, v11
	v_div_fmas_f32 v9, v9, v10, v12
	v_div_fixup_f32 v36, v9, v8, v36
	ds_write_b32 v1, v36 offset:32768
	s_waitcnt vmcnt(16)
	v_mul_f32_e32 v8, 0xbfb8aa3b, v37
	v_exp_f32_e32 v8, v8
	s_nop 0
	v_add_f32_e32 v8, 1.0, v8
	v_div_scale_f32 v9, s[10:11], v8, v8, v37
	v_rcp_f32_e32 v10, v9
	v_div_scale_f32 v11, vcc, v37, v8, v37
	v_fma_f32 v12, -v9, v10, 1.0
	v_fmac_f32_e32 v10, v12, v10
	v_mul_f32_e32 v12, v11, v10
	v_fma_f32 v13, -v9, v12, v11
	v_fmac_f32_e32 v12, v13, v10
	v_fma_f32 v9, -v9, v12, v11
	v_div_fmas_f32 v9, v9, v10, v12
	v_div_fixup_f32 v37, v9, v8, v37
	ds_write_b32 v1, v37 offset:34816
	s_waitcnt vmcnt(15)
	v_mul_f32_e32 v8, 0xbfb8aa3b, v38
	v_exp_f32_e32 v8, v8
	s_nop 0
	v_add_f32_e32 v8, 1.0, v8
	v_div_scale_f32 v9, s[10:11], v8, v8, v38
	v_rcp_f32_e32 v10, v9
	v_div_scale_f32 v11, vcc, v38, v8, v38
	v_fma_f32 v12, -v9, v10, 1.0
	v_fmac_f32_e32 v10, v12, v10
	v_mul_f32_e32 v12, v11, v10
	v_fma_f32 v13, -v9, v12, v11
	v_fmac_f32_e32 v12, v13, v10
	v_fma_f32 v9, -v9, v12, v11
	v_div_fmas_f32 v9, v9, v10, v12
	v_div_fixup_f32 v38, v9, v8, v38
	ds_write_b32 v1, v38 offset:36864
	s_waitcnt vmcnt(14)
	v_mul_f32_e32 v8, 0xbfb8aa3b, v39
	v_exp_f32_e32 v8, v8
	s_nop 0
	v_add_f32_e32 v8, 1.0, v8
	v_div_scale_f32 v9, s[10:11], v8, v8, v39
	v_rcp_f32_e32 v10, v9
	v_div_scale_f32 v11, vcc, v39, v8, v39
	v_fma_f32 v12, -v9, v10, 1.0
	v_fmac_f32_e32 v10, v12, v10
	v_mul_f32_e32 v12, v11, v10
	v_fma_f32 v13, -v9, v12, v11
	v_fmac_f32_e32 v12, v13, v10
	v_fma_f32 v9, -v9, v12, v11
	v_div_fmas_f32 v9, v9, v10, v12
	v_div_fixup_f32 v39, v9, v8, v39
	ds_write_b32 v1, v39 offset:38912
	s_waitcnt vmcnt(13)
	v_mul_f32_e32 v8, 0xbfb8aa3b, v40
	v_exp_f32_e32 v8, v8
	s_nop 0
	v_add_f32_e32 v8, 1.0, v8
	v_div_scale_f32 v9, s[10:11], v8, v8, v40
	v_rcp_f32_e32 v10, v9
	v_div_scale_f32 v11, vcc, v40, v8, v40
	v_fma_f32 v12, -v9, v10, 1.0
	v_fmac_f32_e32 v10, v12, v10
	v_mul_f32_e32 v12, v11, v10
	v_fma_f32 v13, -v9, v12, v11
	v_fmac_f32_e32 v12, v13, v10
	v_fma_f32 v9, -v9, v12, v11
	v_div_fmas_f32 v9, v9, v10, v12
	v_div_fixup_f32 v40, v9, v8, v40
	ds_write_b32 v1, v40 offset:40960
	s_waitcnt vmcnt(12)
	v_mul_f32_e32 v8, 0xbfb8aa3b, v41
	v_exp_f32_e32 v8, v8
	s_nop 0
	v_add_f32_e32 v8, 1.0, v8
	v_div_scale_f32 v9, s[10:11], v8, v8, v41
	v_rcp_f32_e32 v10, v9
	v_div_scale_f32 v11, vcc, v41, v8, v41
	v_fma_f32 v12, -v9, v10, 1.0
	v_fmac_f32_e32 v10, v12, v10
	v_mul_f32_e32 v12, v11, v10
	v_fma_f32 v13, -v9, v12, v11
	v_fmac_f32_e32 v12, v13, v10
	v_fma_f32 v9, -v9, v12, v11
	v_div_fmas_f32 v9, v9, v10, v12
	v_div_fixup_f32 v41, v9, v8, v41
	ds_write_b32 v1, v41 offset:43008
	s_waitcnt vmcnt(11)
	v_mul_f32_e32 v8, 0xbfb8aa3b, v42
	v_exp_f32_e32 v8, v8
	s_nop 0
	v_add_f32_e32 v8, 1.0, v8
	v_div_scale_f32 v9, s[10:11], v8, v8, v42
	v_rcp_f32_e32 v10, v9
	v_div_scale_f32 v11, vcc, v42, v8, v42
	v_fma_f32 v12, -v9, v10, 1.0
	v_fmac_f32_e32 v10, v12, v10
	v_mul_f32_e32 v12, v11, v10
	v_fma_f32 v13, -v9, v12, v11
	v_fmac_f32_e32 v12, v13, v10
	v_fma_f32 v9, -v9, v12, v11
	v_div_fmas_f32 v9, v9, v10, v12
	v_div_fixup_f32 v42, v9, v8, v42
	ds_write_b32 v1, v42 offset:45056
	s_waitcnt vmcnt(10)
	v_mul_f32_e32 v8, 0xbfb8aa3b, v43
	v_exp_f32_e32 v8, v8
	s_nop 0
	v_add_f32_e32 v8, 1.0, v8
	v_div_scale_f32 v9, s[10:11], v8, v8, v43
	v_rcp_f32_e32 v10, v9
	v_div_scale_f32 v11, vcc, v43, v8, v43
	v_fma_f32 v12, -v9, v10, 1.0
	v_fmac_f32_e32 v10, v12, v10
	v_mul_f32_e32 v12, v11, v10
	v_fma_f32 v13, -v9, v12, v11
	v_fmac_f32_e32 v12, v13, v10
	v_fma_f32 v9, -v9, v12, v11
	v_div_fmas_f32 v9, v9, v10, v12
	v_div_fixup_f32 v43, v9, v8, v43
	ds_write_b32 v1, v43 offset:47104
	s_waitcnt vmcnt(9)
	v_mul_f32_e32 v8, 0xbfb8aa3b, v44
	v_exp_f32_e32 v8, v8
	s_nop 0
	v_add_f32_e32 v8, 1.0, v8
	v_div_scale_f32 v9, s[10:11], v8, v8, v44
	v_rcp_f32_e32 v10, v9
	v_div_scale_f32 v11, vcc, v44, v8, v44
	v_fma_f32 v12, -v9, v10, 1.0
	v_fmac_f32_e32 v10, v12, v10
	v_mul_f32_e32 v12, v11, v10
	v_fma_f32 v13, -v9, v12, v11
	v_fmac_f32_e32 v12, v13, v10
	v_fma_f32 v9, -v9, v12, v11
	v_div_fmas_f32 v9, v9, v10, v12
	v_div_fixup_f32 v44, v9, v8, v44
	ds_write_b32 v1, v44 offset:49152
	s_waitcnt vmcnt(8)
	v_mul_f32_e32 v8, 0xbfb8aa3b, v45
	v_exp_f32_e32 v8, v8
	s_nop 0
	v_add_f32_e32 v8, 1.0, v8
	v_div_scale_f32 v9, s[10:11], v8, v8, v45
	v_rcp_f32_e32 v10, v9
	v_div_scale_f32 v11, vcc, v45, v8, v45
	v_fma_f32 v12, -v9, v10, 1.0
	v_fmac_f32_e32 v10, v12, v10
	v_mul_f32_e32 v12, v11, v10
	v_fma_f32 v13, -v9, v12, v11
	v_fmac_f32_e32 v12, v13, v10
	v_fma_f32 v9, -v9, v12, v11
	v_div_fmas_f32 v9, v9, v10, v12
	v_div_fixup_f32 v45, v9, v8, v45
	ds_write_b32 v1, v45 offset:51200
	s_waitcnt vmcnt(7)
	v_mul_f32_e32 v8, 0xbfb8aa3b, v46
	v_exp_f32_e32 v8, v8
	s_nop 0
	v_add_f32_e32 v8, 1.0, v8
	v_div_scale_f32 v9, s[10:11], v8, v8, v46
	v_rcp_f32_e32 v10, v9
	v_div_scale_f32 v11, vcc, v46, v8, v46
	v_fma_f32 v12, -v9, v10, 1.0
	v_fmac_f32_e32 v10, v12, v10
	v_mul_f32_e32 v12, v11, v10
	v_fma_f32 v13, -v9, v12, v11
	v_fmac_f32_e32 v12, v13, v10
	v_fma_f32 v9, -v9, v12, v11
	v_div_fmas_f32 v9, v9, v10, v12
	v_div_fixup_f32 v46, v9, v8, v46
	ds_write_b32 v1, v46 offset:53248
	s_waitcnt vmcnt(6)
	v_mul_f32_e32 v8, 0xbfb8aa3b, v47
	v_exp_f32_e32 v8, v8
	s_nop 0
	v_add_f32_e32 v8, 1.0, v8
	v_div_scale_f32 v9, s[10:11], v8, v8, v47
	v_rcp_f32_e32 v10, v9
	v_div_scale_f32 v11, vcc, v47, v8, v47
	v_fma_f32 v12, -v9, v10, 1.0
	v_fmac_f32_e32 v10, v12, v10
	v_mul_f32_e32 v12, v11, v10
	v_fma_f32 v13, -v9, v12, v11
	v_fmac_f32_e32 v12, v13, v10
	v_fma_f32 v9, -v9, v12, v11
	v_div_fmas_f32 v9, v9, v10, v12
	v_div_fixup_f32 v47, v9, v8, v47
	ds_write_b32 v1, v47 offset:55296
	s_waitcnt vmcnt(5)
	v_mul_f32_e32 v8, 0xbfb8aa3b, v48
	v_exp_f32_e32 v8, v8
	s_nop 0
	v_add_f32_e32 v8, 1.0, v8
	v_div_scale_f32 v9, s[10:11], v8, v8, v48
	v_rcp_f32_e32 v10, v9
	v_div_scale_f32 v11, vcc, v48, v8, v48
	v_fma_f32 v12, -v9, v10, 1.0
	v_fmac_f32_e32 v10, v12, v10
	v_mul_f32_e32 v12, v11, v10
	v_fma_f32 v13, -v9, v12, v11
	v_fmac_f32_e32 v12, v13, v10
	v_fma_f32 v9, -v9, v12, v11
	v_div_fmas_f32 v9, v9, v10, v12
	v_div_fixup_f32 v48, v9, v8, v48
	ds_write_b32 v1, v48 offset:57344
	s_waitcnt vmcnt(4)
	v_mul_f32_e32 v8, 0xbfb8aa3b, v49
	v_exp_f32_e32 v8, v8
	s_nop 0
	v_add_f32_e32 v8, 1.0, v8
	v_div_scale_f32 v9, s[10:11], v8, v8, v49
	v_rcp_f32_e32 v10, v9
	v_div_scale_f32 v11, vcc, v49, v8, v49
	v_fma_f32 v12, -v9, v10, 1.0
	v_fmac_f32_e32 v10, v12, v10
	v_mul_f32_e32 v12, v11, v10
	v_fma_f32 v13, -v9, v12, v11
	v_fmac_f32_e32 v12, v13, v10
	v_fma_f32 v9, -v9, v12, v11
	v_div_fmas_f32 v9, v9, v10, v12
	v_div_fixup_f32 v49, v9, v8, v49
	ds_write_b32 v1, v49 offset:59392
	s_waitcnt vmcnt(3)
	v_mul_f32_e32 v8, 0xbfb8aa3b, v50
	v_exp_f32_e32 v8, v8
	s_nop 0
	v_add_f32_e32 v8, 1.0, v8
	v_div_scale_f32 v9, s[10:11], v8, v8, v50
	v_rcp_f32_e32 v10, v9
	v_div_scale_f32 v11, vcc, v50, v8, v50
	v_fma_f32 v12, -v9, v10, 1.0
	v_fmac_f32_e32 v10, v12, v10
	v_mul_f32_e32 v12, v11, v10
	v_fma_f32 v13, -v9, v12, v11
	v_fmac_f32_e32 v12, v13, v10
	v_fma_f32 v9, -v9, v12, v11
	v_div_fmas_f32 v9, v9, v10, v12
	v_div_fixup_f32 v50, v9, v8, v50
	ds_write_b32 v1, v50 offset:61440
	s_waitcnt vmcnt(2)
	v_mul_f32_e32 v8, 0xbfb8aa3b, v51
	v_exp_f32_e32 v8, v8
	s_nop 0
	v_add_f32_e32 v8, 1.0, v8
	v_div_scale_f32 v9, s[10:11], v8, v8, v51
	v_rcp_f32_e32 v10, v9
	v_div_scale_f32 v11, vcc, v51, v8, v51
	v_fma_f32 v12, -v9, v10, 1.0
	v_fmac_f32_e32 v10, v12, v10
	v_mul_f32_e32 v12, v11, v10
	v_fma_f32 v13, -v9, v12, v11
	v_fmac_f32_e32 v12, v13, v10
	v_fma_f32 v9, -v9, v12, v11
	v_div_fmas_f32 v9, v9, v10, v12
	v_div_fixup_f32 v51, v9, v8, v51
	ds_write_b32 v1, v51 offset:63488
	s_waitcnt vmcnt(1)
	v_mul_f32_e32 v8, 0xbfb8aa3b, v52
	v_exp_f32_e32 v8, v8
	s_nop 0
	v_add_f32_e32 v8, 1.0, v8
	v_div_scale_f32 v9, s[10:11], v8, v8, v52
	v_rcp_f32_e32 v10, v9
	v_div_scale_f32 v11, vcc, v52, v8, v52
	v_fma_f32 v12, -v9, v10, 1.0
	v_fmac_f32_e32 v10, v12, v10
	v_mul_f32_e32 v12, v11, v10
	v_fma_f32 v13, -v9, v12, v11
	v_fmac_f32_e32 v12, v13, v10
	v_fma_f32 v9, -v9, v12, v11
	v_div_fmas_f32 v9, v9, v10, v12
	v_div_fixup_f32 v52, v9, v8, v52
	ds_write_b32 v3, v52
	s_waitcnt vmcnt(0)
	v_mul_f32_e32 v8, 0xbfb8aa3b, v53
	v_exp_f32_e32 v8, v8
	s_nop 0
	v_add_f32_e32 v8, 1.0, v8
	v_div_scale_f32 v9, s[10:11], v8, v8, v53
	v_rcp_f32_e32 v10, v9
	v_div_scale_f32 v11, vcc, v53, v8, v53
	v_fma_f32 v12, -v9, v10, 1.0
	v_fmac_f32_e32 v10, v12, v10
	v_mul_f32_e32 v12, v11, v10
	v_fma_f32 v13, -v9, v12, v11
	v_fmac_f32_e32 v12, v13, v10
	v_fma_f32 v9, -v9, v12, v11
	v_div_fmas_f32 v9, v9, v10, v12
	v_div_fixup_f32 v53, v9, v8, v53
	ds_write_b32 v3, v53 offset:2048
	s_mul_hi_u32 s3, s2, 0xaaaaaaab
	s_lshr_b32 s3, s3, 6
	s_mul_i32 s4, s3, 0x60
	s_sub_i32 s4, s2, s4
	s_lshl_b32 s4, s4, 6
	s_mul_i32 s7, s3, 0x1800000
	s_mov_b32 s5, 0
	s_mul_hi_u32 s6, s3, 0x1800000
	s_add_u32 s8, s44, s7
	s_addc_u32 s9, s45, s6
	s_lshl_b64 s[6:7], s[4:5], 2
	v_and_b32_e32 v1, 60, v2
	s_add_u32 s6, s8, s6
	s_addc_u32 s7, s9, s7
	v_lshlrev_b32_e32 v18, 2, v1
	v_mov_b32_e32 v19, 0
	v_lshl_add_u64 v[54:55], s[6:7], 0, v[18:19]
	v_readlane_b32 s6, v254, 6
	v_lshrrev_b32_e32 v2, 4, v250
	s_mov_b32 s8, s6
	s_lshl_b32 s6, s6, 7
	v_or3_b32 v91, v2, s6, 28
	s_lshl_b32 s6, s8, 9
	s_add_i32 s6, s6, 0
	v_lshl_add_u32 v125, v2, 2, s6
	s_movk_i32 s6, 0x6000
	v_mov_b32_e32 v18, v19
	v_mov_b32_e32 v24, v19
	v_mov_b32_e32 v25, v19
	v_mov_b32_e32 v22, v19
	v_mov_b32_e32 v23, v19
	v_mov_b32_e32 v20, v19
	v_mov_b32_e32 v21, v19
	v_mov_b32_e32 v28, v19
	v_mov_b32_e32 v29, v19
	v_mov_b32_e32 v26, v19
	v_mov_b32_e32 v27, v19
	v_mov_b32_e32 v32, v19
	v_mov_b32_e32 v33, v19
	v_mov_b32_e32 v30, v19
	v_mov_b32_e32 v31, v19
	v_mov_b32_e32 v36, v19
	v_mov_b32_e32 v37, v19
	v_mov_b32_e32 v34, v19
	v_mov_b32_e32 v35, v19
	v_mov_b32_e32 v40, v19
	v_mov_b32_e32 v41, v19
	v_mov_b32_e32 v38, v19
	v_mov_b32_e32 v39, v19
	v_mov_b32_e32 v44, v19
	v_mov_b32_e32 v45, v19
	v_mov_b32_e32 v42, v19
	v_mov_b32_e32 v43, v19
	v_mov_b32_e32 v48, v19
	v_mov_b32_e32 v49, v19
	v_mov_b32_e32 v46, v19
	v_mov_b32_e32 v47, v19
	v_mov_b32_e32 v52, v19
	v_mov_b32_e32 v53, v19
	v_mov_b32_e32 v50, v19
	v_mov_b32_e32 v51, v19
	v_mov_b32_e32 v58, v19
	v_mov_b32_e32 v59, v19
	v_mov_b32_e32 v56, v19
	v_mov_b32_e32 v57, v19
	v_mov_b32_e32 v62, v19
	v_mov_b32_e32 v63, v19
	v_mov_b32_e32 v60, v19
	v_mov_b32_e32 v61, v19
	v_mov_b32_e32 v66, v19
	v_mov_b32_e32 v67, v19
	v_mov_b32_e32 v64, v19
	v_mov_b32_e32 v65, v19
	v_mov_b32_e32 v70, v19
	v_mov_b32_e32 v71, v19
	v_mov_b32_e32 v68, v19
	v_mov_b32_e32 v69, v19
	v_mov_b32_e32 v74, v19
	v_mov_b32_e32 v75, v19
	v_mov_b32_e32 v72, v19
	v_mov_b32_e32 v73, v19
	v_mov_b32_e32 v78, v19
	v_mov_b32_e32 v79, v19
	v_mov_b32_e32 v76, v19
	v_mov_b32_e32 v77, v19
	v_mov_b32_e32 v82, v19
	v_mov_b32_e32 v83, v19
	v_mov_b32_e32 v80, v19
	v_mov_b32_e32 v81, v19
	v_mov_b32_e32 v86, v19
	v_mov_b32_e32 v87, v19
	v_mov_b32_e32 v84, v19
	v_mov_b32_e32 v85, v19
	s_waitcnt lgkmcnt(0)
	s_barrier
	v_readlane_b32 s7, v254, 7

	.amdhsa_kernel _Z9trunk_fwd4Args
		.amdhsa_group_segment_fixed_size 0
		.amdhsa_private_segment_fixed_size 0
		.amdhsa_kernarg_size 480
		.amdhsa_user_sgpr_count 2
		.amdhsa_user_sgpr_dispatch_ptr 0
		.amdhsa_user_sgpr_queue_ptr 0
		.amdhsa_user_sgpr_kernarg_segment_ptr 1
		.amdhsa_user_sgpr_dispatch_id 0
		.amdhsa_user_sgpr_kernarg_preload_length 0
		.amdhsa_user_sgpr_kernarg_preload_offset 0
		.amdhsa_user_sgpr_private_segment_size 0
		.amdhsa_uses_dynamic_stack 0
		.amdhsa_enable_private_segment 0
		.amdhsa_system_sgpr_workgroup_id_x 1
		.amdhsa_system_sgpr_workgroup_id_y 0
		.amdhsa_system_sgpr_workgroup_id_z 0
		.amdhsa_system_sgpr_workgroup_info 0
		.amdhsa_system_vgpr_workitem_id 0
		.amdhsa_next_free_vgpr 255
		.amdhsa_next_free_sgpr 102
		.amdhsa_accum_offset 256
		.amdhsa_reserve_vcc 1
		.amdhsa_float_round_mode_32 0
		.amdhsa_float_round_mode_16_64 0
		.amdhsa_float_denorm_mode_32 3
		.amdhsa_float_denorm_mode_16_64 3
		.amdhsa_dx10_clamp 1
		.amdhsa_ieee_mode 1
		.amdhsa_fp16_overflow 0
		.amdhsa_tg_split 0
		.amdhsa_exception_fp_ieee_invalid_op 0
		.amdhsa_exception_fp_denorm_src 0
		.amdhsa_exception_fp_ieee_div_zero 0
		.amdhsa_exception_fp_ieee_overflow 0
		.amdhsa_exception_fp_ieee_underflow 0
		.amdhsa_exception_fp_ieee_inexact 0
		.amdhsa_exception_int_div_zero 0
	.end_amdhsa_kernel

amdhsa.kernels:
  - .agpr_count:     0
    .args:
      - .offset:         0
        .size:           224
        .value_kind:     by_value
      - .offset:         224
        .size:           4
        .value_kind:     hidden_block_count_x
      - .offset:         228
        .size:           4
        .value_kind:     hidden_block_count_y
      - .offset:         232
        .size:           4
        .value_kind:     hidden_block_count_z
      - .offset:         236
        .size:           2
        .value_kind:     hidden_group_size_x
      - .offset:         238
        .size:           2
        .value_kind:     hidden_group_size_y
      - .offset:         240
        .size:           2
        .value_kind:     hidden_group_size_z
      - .offset:         242
        .size:           2
        .value_kind:     hidden_remainder_x
      - .offset:         244
        .size:           2
        .value_kind:     hidden_remainder_y
      - .offset:         246
        .size:           2
        .value_kind:     hidden_remainder_z
      - .offset:         264
        .size:           8
        .value_kind:     hidden_global_offset_x
      - .offset:         272
        .size:           8
        .value_kind:     hidden_global_offset_y
      - .offset:         280
        .size:           8
        .value_kind:     hidden_global_offset_z
      - .offset:         288
        .size:           2
        .value_kind:     hidden_grid_dims
      - .offset:         344
        .size:           4
        .value_kind:     hidden_dynamic_lds_size
    .group_segment_fixed_size: 0
    .kernarg_segment_align: 8
    .kernarg_segment_size: 480
    .language:       OpenCL C
    .language_version:
      - 2
      - 0
    .max_flat_workgroup_size: 512
    .name:           _Z9trunk_fwd4Args
    .private_segment_fixed_size: 0
    .sgpr_count:     108
    .sgpr_spill_count: 50
    .symbol:         _Z9trunk_fwd4Args.kd
    .uniform_work_group_size: 1
    .uses_dynamic_stack: false
    .vgpr_count:     255
    .vgpr_spill_count: 0
    .wavefront_size: 64
